# baseline (speedup 1.0000x reference)
.LBB1_25:
	s_or_b64 exec, exec, s[8:9]
	s_load_dwordx8 s[12:19], s[0:1], 0x10
	v_and_b32_e32 v25, 63, v0
	v_mov_b32_e32 v36, 0
	v_mbcnt_lo_u32_b32 v35, -1, 0
	v_mov_b32_e32 v34, 0
	v_mov_b32_e32 v33, 0
	v_mov_b32_e32 v37, 0
	s_waitcnt lgkmcnt(0)
	s_barrier
	s_and_saveexec_b64 s[0:1], s[4:5]
	s_cbranch_execz .LBB1_29
	ds_read_b32 v36, v1 offset:10832
	s_waitcnt lgkmcnt(0)
	v_mov_b32_e32 v37, v36
	s_nop 1
	v_add_u32_dpp v37, v37, v37 row_shr:1 row_mask:0xf bank_mask:0xf
	s_nop 1
	v_add_u32_dpp v37, v37, v37 row_shr:2 row_mask:0xf bank_mask:0xf
	s_nop 1
	v_add_u32_dpp v37, v37, v37 row_shr:4 row_mask:0xf bank_mask:0xf
	s_nop 1
	v_add_u32_dpp v37, v37, v37 row_shr:8 row_mask:0xf bank_mask:0xf
	s_nop 1
	v_add_u32_dpp v37, v37, v37 row_bcast:15 row_mask:0xa bank_mask:0xf
	s_nop 1
	v_add_u32_dpp v37, v37, v37 row_bcast:31 row_mask:0xc bank_mask:0xf
	v_cmp_eq_u32_e32 vcc, 63, v25
	s_and_saveexec_b64 s[8:9], vcc
	v_lshrrev_b32_e32 v33, 4, v0
	v_and_b32_e32 v33, 12, v33
	ds_write_b32 v33, v37 offset:10824
	s_or_b64 exec, exec, s[8:9]
	v_min_i32_e32 v34, 63, v36
	v_lshlrev_b32_e32 v33, 2, v34
	v_sub_u32_e32 v33, 0, v33
	v_mov_b32_e32 v38, 1
	ds_add_rtn_u32 v33, v33, v38 offset:12108
	v_sub_u32_e32 v34, 63, v34

.LBB1_32:
	s_or_b64 exec, exec, s[0:1]
	s_and_saveexec_b64 s[0:1], s[6:7]
	s_cbranch_execz .LBB1_34
	ds_read_b32 v36, v1 offset:11856
	s_waitcnt lgkmcnt(0)
	v_mov_b32_e32 v35, v36
	s_nop 1
	v_add_u32_dpp v35, v35, v35 row_shr:1 row_mask:0xf bank_mask:0xf
	s_nop 1
	v_add_u32_dpp v35, v35, v35 row_shr:2 row_mask:0xf bank_mask:0xf
	s_nop 1
	v_add_u32_dpp v35, v35, v35 row_shr:4 row_mask:0xf bank_mask:0xf
	s_nop 1
	v_add_u32_dpp v35, v35, v35 row_shr:8 row_mask:0xf bank_mask:0xf
	s_nop 1
	v_add_u32_dpp v35, v35, v35 row_bcast:15 row_mask:0xa bank_mask:0xf
	s_nop 1
	v_add_u32_dpp v35, v35, v35 row_bcast:31 row_mask:0xc bank_mask:0xf
	v_sub_u32_e32 v35, v35, v36
	ds_write_b32 v1, v35 offset:11856
